# P2b scan loop: dequeue the next queue id after the scan item instead of at its start (scan WGs no longer reserve a heavy early indexer item)
# speedup vs baseline: 1.0379x; 1.0048x over previous
.LBB0_549:
	v_mov_b32_e32 v1, 0
	s_ashr_i32 s10, s33, 3
	s_bfe_u32 s36, s33, 0x20001
	v_mov_b32_e32 v3, v0
	s_lshl_b32 s34, s10, 7
	s_lshl_b32 s35, s36, 5
	s_or_b32 s28, s35, s34
	v_readfirstlane_b32 s4, v3
	s_ashr_i32 s4, s4, 6
	s_add_i32 s5, s28, 0xfffffe00
	s_ashr_i32 s29, s28, 31
	s_cmpk_lt_i32 s28, 0x200
	s_cselect_b32 s13, s29, 0
	s_cselect_b32 s12, s28, s5
	s_cselect_b32 s5, s68, s58
	s_cselect_b32 s11, s3, s43
	s_lshl_b64 s[12:13], s[12:13], 16
	v_and_b32_e32 v4, 63, v3
	s_add_u32 s12, s11, s12
	s_addc_u32 s13, s5, s13
	v_lshlrev_b32_e32 v76, 4, v4
	s_ashr_i32 s5, s4, 31
	s_add_i32 s16, s4, 8
	v_lshl_add_u64 v[6:7], s[12:13], 0, v[76:77]
	s_lshl_b64 s[12:13], s[4:5], 10
	s_lshl_b32 s61, s4, 10
	s_ashr_i32 s17, s16, 31
	v_lshl_add_u64 v[8:9], v[6:7], 0, s[12:13]
	s_add_i32 s5, s61, 0
	s_mov_b32 s11, m0
	s_mov_b32 m0, s5
	s_nop 0
	global_load_lds_dwordx4 v[8:9], off
	s_mov_b32 m0, s11
	s_lshl_b64 s[14:15], s[16:17], 10
	s_lshl_b32 s62, s16, 10
	s_add_i32 s18, s4, 16
	v_lshl_add_u64 v[8:9], v[6:7], 0, s[14:15]
	s_add_i32 s11, s62, 0
	s_mov_b32 s16, m0
	s_mov_b32 m0, s11
	s_nop 0
	global_load_lds_dwordx4 v[8:9], off
	s_mov_b32 m0, s16
	s_ashr_i32 s19, s18, 31
	s_lshl_b64 s[16:17], s[18:19], 10
	s_lshl_b32 s63, s18, 10
	s_add_i32 s20, s4, 24
	v_lshl_add_u64 v[8:9], v[6:7], 0, s[16:17]
	s_add_i32 s11, s63, 0
	s_mov_b32 s18, m0
	s_mov_b32 m0, s11
	s_nop 0
	global_load_lds_dwordx4 v[8:9], off
	s_mov_b32 m0, s18
	s_ashr_i32 s21, s20, 31
	s_lshl_b64 s[18:19], s[20:21], 10
	s_lshl_b32 s69, s20, 10
	s_add_i32 s22, s4, 32
	v_lshl_add_u64 v[8:9], v[6:7], 0, s[18:19]
	s_add_i32 s11, s69, 0
	s_mov_b32 s20, m0
	s_mov_b32 m0, s11
	s_nop 0
	global_load_lds_dwordx4 v[8:9], off
	s_mov_b32 m0, s20
	s_ashr_i32 s23, s22, 31
	s_lshl_b64 s[20:21], s[22:23], 10
	s_lshl_b32 s70, s22, 10
	s_add_i32 s24, s4, 40
	v_lshl_add_u64 v[8:9], v[6:7], 0, s[20:21]
	s_add_i32 s11, s70, 0
	s_mov_b32 s22, m0
	s_mov_b32 m0, s11
	s_nop 0
	global_load_lds_dwordx4 v[8:9], off
	s_mov_b32 m0, s22
	s_ashr_i32 s25, s24, 31
	s_lshl_b64 s[22:23], s[24:25], 10
	s_lshl_b32 s71, s24, 10
	s_add_i32 s26, s4, 48
	v_lshl_add_u64 v[8:9], v[6:7], 0, s[22:23]
	s_add_i32 s11, s71, 0
	s_mov_b32 s24, m0
	s_mov_b32 m0, s11
	s_nop 0
	global_load_lds_dwordx4 v[8:9], off
	s_mov_b32 m0, s24
	s_ashr_i32 s27, s26, 31
	s_lshl_b64 s[24:25], s[26:27], 10
	s_lshl_b32 s72, s26, 10
	s_add_i32 s40, s4, 56
	v_lshl_add_u64 v[8:9], v[6:7], 0, s[24:25]
	s_add_i32 s11, s72, 0
	s_mov_b32 s26, m0
	s_mov_b32 m0, s11
	s_nop 0
	global_load_lds_dwordx4 v[8:9], off
	s_mov_b32 m0, s26
	s_ashr_i32 s41, s40, 31
	s_lshl_b32 s73, s40, 10
	s_lshl_b64 s[30:31], s[28:29], 13
	s_lshl_b64 s[26:27], s[40:41], 10
	s_add_i32 s11, s73, 0
	v_lshl_add_u64 v[6:7], v[6:7], 0, s[26:27]
	s_mov_b32 s29, m0
	s_mov_b32 m0, s11
	s_nop 0
	global_load_lds_dwordx4 v[6:7], off
	s_mov_b32 m0, s29
	s_add_u32 s11, s6, s30
	s_addc_u32 s29, s7, s31
	s_add_u32 s30, s11, s12
	s_addc_u32 s31, s29, s13
	v_lshl_add_u64 v[6:7], s[30:31], 0, v[76:77]
	s_add_i32 s5, s5, 0x10000
	s_mov_b32 s11, m0
	s_mov_b32 m0, s5
	s_nop 0
	global_load_lds_dwordx4 v[6:7], off
	s_mov_b32 m0, s11
	v_cmp_gt_i32_e32 vcc, 32, v3
	s_and_saveexec_b64 s[30:31], vcc
	s_cbranch_execz .LBB0_555
	v_add_u32_e32 v6, s28, v3
	v_ashrrev_i32_e32 v7, 31, v6
	v_lshl_add_u64 v[6:7], v[6:7], 2, s[0:1]
	global_load_dword v5, v[6:7], off
	v_lshl_add_u32 v6, v3, 2, 0
	v_add_u32_e32 v6, 0x24000, v6
	s_waitcnt vmcnt(0)
	ds_write_b32 v6, v5

.LBB0_562:
	s_waitcnt vmcnt(0)
	s_waitcnt lgkmcnt(0)
	s_barrier
	s_barrier
	s_and_saveexec_b64 s[4:5], s[94:95]
	s_cbranch_execz .LBB0_548
	v_mov_b32_e32 v3, 1
	v_readlane_b32 s12, v252, 10
	v_readlane_b32 s13, v252, 11
	s_nop 4
	global_atomic_add v1, v77, v3, s[12:13] sc0
	s_waitcnt vmcnt(0)
	v_mov_b32_e32 v3, s42
	ds_write_b32 v3, v1
	s_branch .LBB0_548
